# speedup vs baseline: 1.0040x; 1.0040x over previous
.Lstag_loop_p3:
	s_sleep 44
	s_add_i32 s20, s20, -1
	s_cmp_lg_u32 s20, 0
	s_cbranch_scc1 .Lstag_loop_p3
